# speedup vs baseline: 1.0285x; 1.0285x over previous
.LBB3_1:
	s_lshl_b32 s12, s3, 15
	v_or_b32_e32 v67, s12, v65
	s_waitcnt lgkmcnt(0)
	v_mfma_f32_16x16x32_f16 v[54:57], v[22:25], v[10:13], v[54:57]
	ds_read_b128 v[68:71], v67 offset:1024
	ds_read_b128 v[72:75], v67 offset:3072
	v_or_b32_e32 v67, s12, v64
	v_mfma_f32_16x16x32_f16 v[50:53], v[18:21], v[10:13], v[50:53]
	ds_read_b128 v[76:79], v67 offset:17408
	ds_read_b128 v[80:83], v67 offset:19456
	s_add_i32 s3, s3, 1
	v_mfma_f32_16x16x32_f16 v[46:49], v[26:29], v[10:13], v[46:49]
	ds_read_b128 v[84:87], v67 offset:21504
	ds_read_b128 v[88:91], v67 offset:23552
	v_mfma_f32_16x16x32_f16 v[42:45], v[14:17], v[10:13], v[42:45]
	v_mfma_f32_16x16x32_f16 v[38:41], v[22:25], v[6:9], v[38:41]
	v_mfma_f32_16x16x32_f16 v[34:37], v[18:21], v[6:9], v[34:37]
	v_mfma_f32_16x16x32_f16 v[30:33], v[26:29], v[6:9], v[30:33]
	v_mfma_f32_16x16x32_f16 v[2:5], v[14:17], v[6:9], v[2:5]
	s_waitcnt vmcnt(4) lgkmcnt(0)
	s_barrier
	v_or_b32_e32 v10, s12, v66
	v_lshl_add_u64 v[6:7], v[60:61], 0, s[4:5]
	v_readfirstlane_b32 s12, v10
	v_lshl_add_u64 v[8:9], v[6:7], 0, s[6:7]
	s_mov_b32 m0, s12
	s_nop 0
	global_load_lds_dwordx4 v[8:9], off
	v_or_b32_e32 v8, 0x2000, v10
	v_lshl_add_u64 v[6:7], v[6:7], 0, s[10:11]
	v_readfirstlane_b32 s12, v8
	s_mov_b32 m0, s12
	v_or_b32_e32 v11, 0x4000, v10
	global_load_lds_dwordx4 v[6:7], off
	v_lshl_add_u64 v[6:7], v[58:59], 0, s[4:5]
	v_readfirstlane_b32 s12, v11
	v_lshl_add_u64 v[8:9], v[6:7], 0, s[6:7]
	s_mov_b32 m0, s12
	v_lshl_add_u64 v[6:7], v[6:7], 0, s[10:11]
	global_load_lds_dwordx4 v[8:9], off
	v_or_b32_e32 v8, 0x6000, v10
	s_cmp_lg_u32 s3, 3
	v_readfirstlane_b32 s12, v8
	s_mov_b32 m0, s12
	s_cselect_b32 s3, s3, 0
	global_load_lds_dwordx4 v[6:7], off
	s_lshl_b32 s12, s3, 15
	v_or_b32_e32 v6, s12, v65
	v_or_b32_e32 v14, s12, v64
	s_waitcnt lgkmcnt(0)
	v_mfma_f32_16x16x32_f16 v[54:57], v[76:79], v[68:71], v[54:57]
	ds_read_b128 v[10:13], v6
	ds_read_b128 v[6:9], v6 offset:2048
	v_mfma_f32_16x16x32_f16 v[50:53], v[80:83], v[68:71], v[50:53]
	ds_read_b128 v[22:25], v14 offset:16384
	ds_read_b128 v[18:21], v14 offset:18432
	v_mfma_f32_16x16x32_f16 v[46:49], v[84:87], v[68:71], v[46:49]
	ds_read_b128 v[26:29], v14 offset:20480
	ds_read_b128 v[14:17], v14 offset:22528
	v_mfma_f32_16x16x32_f16 v[42:45], v[88:91], v[68:71], v[42:45]
	v_mfma_f32_16x16x32_f16 v[38:41], v[76:79], v[72:75], v[38:41]
	v_mfma_f32_16x16x32_f16 v[34:37], v[80:83], v[72:75], v[34:37]
	v_mfma_f32_16x16x32_f16 v[30:33], v[84:87], v[72:75], v[30:33]
	v_mfma_f32_16x16x32_f16 v[2:5], v[88:91], v[72:75], v[2:5]
	s_add_u32 s4, s4, 0x80
	s_addc_u32 s5, s5, 0
	s_cmpk_eq_i32 s4, 0x680
	s_cbranch_scc0 .LBB3_1
	s_waitcnt lgkmcnt(0)
	v_mfma_f32_16x16x32_f16 v[54:57], v[22:25], v[10:13], v[54:57]
	ds_read_b128 v[58:61], v65 offset:33792
	ds_read_b128 v[66:69], v65 offset:35840
	v_mfma_f32_16x16x32_f16 v[50:53], v[18:21], v[10:13], v[50:53]
	ds_read_b128 v[70:73], v64 offset:50176
	ds_read_b128 v[74:77], v64 offset:52224
	v_mfma_f32_16x16x32_f16 v[46:49], v[26:29], v[10:13], v[46:49]
	ds_read_b128 v[78:81], v64 offset:54272
	ds_read_b128 v[82:85], v64 offset:56320
	v_mfma_f32_16x16x32_f16 v[10:13], v[14:17], v[10:13], v[42:45]
	v_mfma_f32_16x16x32_f16 v[22:25], v[22:25], v[6:9], v[38:41]
	v_mfma_f32_16x16x32_f16 v[18:21], v[18:21], v[6:9], v[34:37]
	v_mfma_f32_16x16x32_f16 v[26:29], v[26:29], v[6:9], v[30:33]
	v_mfma_f32_16x16x32_f16 v[2:5], v[14:17], v[6:9], v[2:5]
	v_or_b32_e32 v14, 0x10000, v65
	s_nop 0
	v_add_u32_e32 v30, 0x10800, v65
	s_waitcnt vmcnt(4) lgkmcnt(0)
	s_barrier
	s_waitcnt lgkmcnt(0)
	v_mfma_f32_16x16x32_f16 v[6:9], v[70:73], v[58:61], v[54:57]
	ds_read_b128 v[14:17], v14
	ds_read_b128 v[30:33], v30
	v_or_b32_e32 v38, 0x14000, v64
	v_mfma_f32_16x16x32_f16 v[34:37], v[74:77], v[58:61], v[50:53]
	v_add_u32_e32 v42, 0x14800, v64
	v_add_u32_e32 v54, 0x15800, v64
	ds_read_b128 v[38:41], v38
	v_add_u32_e32 v50, 0x15000, v64
	ds_read_b128 v[42:45], v42
	v_mfma_f32_16x16x32_f16 v[46:49], v[78:81], v[58:61], v[46:49]
	ds_read_b128 v[50:53], v50
	ds_read_b128 v[54:57], v54
	v_mfma_f32_16x16x32_f16 v[10:13], v[82:85], v[58:61], v[10:13]
	v_mfma_f32_16x16x32_f16 v[22:25], v[70:73], v[66:69], v[22:25]
	v_mfma_f32_16x16x32_f16 v[18:21], v[74:77], v[66:69], v[18:21]
	v_mfma_f32_16x16x32_f16 v[26:29], v[78:81], v[66:69], v[26:29]
	v_mfma_f32_16x16x32_f16 v[2:5], v[82:85], v[66:69], v[2:5]
	v_add_u32_e32 v58, 0x10400, v65
	v_add_u32_e32 v66, 0x10c00, v65
	v_add_u32_e32 v70, 0x14400, v64
	v_add_u32_e32 v74, 0x14c00, v64
	v_add_u32_e32 v78, 0x15400, v64
	v_add_u32_e32 v82, 0x15c00, v64
	s_waitcnt lgkmcnt(0)
	v_mfma_f32_16x16x32_f16 v[6:9], v[38:41], v[14:17], v[6:9]
	ds_read_b128 v[58:61], v58
	ds_read_b128 v[66:69], v66
	v_mfma_f32_16x16x32_f16 v[34:37], v[42:45], v[14:17], v[34:37]
	ds_read_b128 v[70:73], v70
	ds_read_b128 v[74:77], v74
	v_mfma_f32_16x16x32_f16 v[46:49], v[50:53], v[14:17], v[46:49]
	ds_read_b128 v[78:81], v78
	ds_read_b128 v[82:85], v82
	v_mfma_f32_16x16x32_f16 v[10:13], v[54:57], v[14:17], v[10:13]
	v_mfma_f32_16x16x32_f16 v[14:17], v[38:41], v[30:33], v[22:25]
	v_mfma_f32_16x16x32_f16 v[18:21], v[42:45], v[30:33], v[18:21]
	v_mfma_f32_16x16x32_f16 v[22:25], v[50:53], v[30:33], v[26:29]
	v_mfma_f32_16x16x32_f16 v[2:5], v[54:57], v[30:33], v[2:5]
	s_waitcnt vmcnt(0) lgkmcnt(0)
	s_waitcnt lgkmcnt(0)
	v_mfma_f32_16x16x32_f16 v[6:9], v[70:73], v[58:61], v[6:9]
	s_barrier
	ds_read_b128 v[26:29], v65
	ds_read_b128 v[30:33], v65 offset:2048
	v_mfma_f32_16x16x32_f16 v[34:37], v[74:77], v[58:61], v[34:37]
	ds_read_b128 v[38:41], v64 offset:16384
	ds_read_b128 v[42:45], v64 offset:18432
	v_mfma_f32_16x16x32_f16 v[46:49], v[78:81], v[58:61], v[46:49]
	ds_read_b128 v[50:53], v64 offset:20480
	ds_read_b128 v[54:57], v64 offset:22528
	v_mfma_f32_16x16x32_f16 v[10:13], v[82:85], v[58:61], v[10:13]
	v_mfma_f32_16x16x32_f16 v[14:17], v[70:73], v[66:69], v[14:17]
	v_mfma_f32_16x16x32_f16 v[18:21], v[74:77], v[66:69], v[18:21]
	v_mfma_f32_16x16x32_f16 v[22:25], v[78:81], v[66:69], v[22:25]
	v_mfma_f32_16x16x32_f16 v[2:5], v[82:85], v[66:69], v[2:5]
	s_waitcnt lgkmcnt(0)
	v_mfma_f32_16x16x32_f16 v[6:9], v[38:41], v[26:29], v[6:9]
	ds_read_b128 v[58:61], v64 offset:19456
	s_lshl_b64 s[0:1], s[0:1], 2
	v_lshl_add_u32 v63, v63, 5, s2
	v_mfma_f32_16x16x32_f16 v[34:37], v[42:45], v[26:29], v[34:37]
	s_add_u32 s0, s8, s0
	v_and_or_b32 v0, v0, 15, v63
	s_addc_u32 s1, s9, s1
	v_mfma_f32_16x16x32_f16 v[46:49], v[50:53], v[26:29], v[46:49]
	v_and_b32_e32 v1, 12, v1
	v_mfma_f32_16x16x32_f16 v[10:13], v[54:57], v[26:29], v[10:13]
	ds_read_b128 v[26:29], v65 offset:1024
	v_mfma_f32_16x16x32_f16 v[14:17], v[38:41], v[30:33], v[14:17]
	ds_read_b128 v[38:41], v65 offset:3072
	v_mfma_f32_16x16x32_f16 v[18:21], v[42:45], v[30:33], v[18:21]
	ds_read_b128 v[42:45], v64 offset:17408
	v_mfma_f32_16x16x32_f16 v[22:25], v[50:53], v[30:33], v[22:25]
	ds_read_b128 v[50:53], v64 offset:21504
	ds_read_b128 v[64:67], v64 offset:23552
	v_mfma_f32_16x16x32_f16 v[2:5], v[54:57], v[30:33], v[2:5]
	v_lshlrev_b32_e32 v54, 8, v62
	v_mov_b32_e32 v55, 0
	v_lshl_add_u64 v[56:57], s[0:1], 0, v[54:55]
	s_waitcnt lgkmcnt(0)
	v_mfma_f32_16x16x32_f16 v[6:9], v[42:45], v[26:29], v[6:9]
	v_lshlrev_b32_e32 v54, 2, v1
	v_ashrrev_i32_e32 v1, 31, v0
	v_mfma_f32_16x16x32_f16 v[10:13], v[64:67], v[26:29], v[10:13]
	v_mfma_f32_16x16x32_f16 v[30:33], v[58:61], v[26:29], v[34:37]
	v_mfma_f32_16x16x32_f16 v[34:37], v[50:53], v[26:29], v[46:49]
	s_nop 2
	v_lshlrev_b64 v[48:49], 12, v[0:1]
	v_or_b32_e32 v0, 16, v0
	v_lshl_add_u64 v[46:47], v[56:57], 0, v[54:55]
	v_ashrrev_i32_e32 v1, 31, v0
	v_lshl_add_u64 v[26:27], v[46:47], 0, v[48:49]
	v_lshlrev_b64 v[0:1], 12, v[0:1]
	global_store_dwordx4 v[26:27], v[6:9], off sc1
	global_store_dwordx4 v[26:27], v[10:13], off offset:192 sc1
	global_store_dwordx4 v[26:27], v[30:33], off offset:64 sc1
	v_mfma_f32_16x16x32_f16 v[6:9], v[42:45], v[38:41], v[14:17]
	global_store_dwordx4 v[26:27], v[34:37], off offset:128 sc1
	v_mfma_f32_16x16x32_f16 v[10:13], v[58:61], v[38:41], v[18:21]
	s_nop 2
	v_lshl_add_u64 v[18:19], v[46:47], 0, v[0:1]
	v_mfma_f32_16x16x32_f16 v[14:17], v[50:53], v[38:41], v[22:25]
	s_nop 0
	global_store_dwordx4 v[18:19], v[6:9], off sc1
	s_nop 0
	global_store_dwordx4 v[18:19], v[10:13], off offset:64 sc1
	v_mfma_f32_16x16x32_f16 v[0:3], v[64:67], v[38:41], v[2:5]
	s_nop 2
	global_store_dwordx4 v[18:19], v[14:17], off offset:128 sc1
	s_nop 3
	global_store_dwordx4 v[18:19], v[0:3], off offset:192 sc1
	s_endpgm
